# bundle5: + up-GEMM SwiGLU epilogue re-emitted stage-wise (8 independent elements per stage, no register shuffles)
# baseline (speedup 1.0000x reference)
.LBB0_834:
	v_mov_b32_e32 v1, v207
	v_mov_b32_e32 v0, v206
	s_lshl_b32 s11, s16, 8
	s_add_i32 s11, s11, s36
	v_add_u32_e32 v0, s11, v0
	s_lshl_b32 s11, s18, 7
	s_and_b32 s11, s11, 0x180
	s_or_b32 s11, s11, s37
	v_lshl_add_u32 v2, v1, 3, s11
	v_ashrrev_i32_e32 v3, 31, v2
	s_mov_b64 s[16:17], -1
	v_ashrrev_i32_e32 v1, 31, v0
	v_lshlrev_b64 v[0:1], 9, v[0:1]
	v_lshl_add_u64 v[0:1], s[64:65], 0, v[0:1]
	v_lshl_add_u64 v[0:1], v[0:1], 0, v[2:3]
	s_mov_b32 s101, 0
	v_mul_f32_e32 v230, s48, v190
	v_mul_f32_e32 v231, s48, v191
	v_mul_f32_e32 v232, s48, v192
	v_mul_f32_e32 v233, s48, v193
	v_mul_f32_e32 v234, s48, v186
	v_mul_f32_e32 v235, s48, v187
	v_mul_f32_e32 v236, s48, v188
	v_mul_f32_e32 v237, s48, v189
	v_mul_f32_e32 v238, s48, v182
	v_mul_f32_e32 v239, s48, v183
	v_mul_f32_e32 v240, s48, v184
	v_mul_f32_e32 v241, s48, v185
	v_mul_f32_e32 v242, s48, v178
	v_mul_f32_e32 v243, s48, v179
	v_mul_f32_e32 v244, s48, v180
	v_mul_f32_e32 v245, s48, v181
	v_mul_f32_e32 v246, 0xbfb8aa3b, v230
	v_mul_f32_e32 v247, 0xbfb8aa3b, v231
	v_mul_f32_e32 v248, 0xbfb8aa3b, v232
	v_mul_f32_e32 v249, 0xbfb8aa3b, v233
	v_mul_f32_e32 v250, 0xbfb8aa3b, v234
	v_mul_f32_e32 v251, 0xbfb8aa3b, v235
	v_mul_f32_e32 v252, 0xbfb8aa3b, v236
	v_mul_f32_e32 v253, 0xbfb8aa3b, v237
	v_exp_f32_e32 v246, v246
	v_exp_f32_e32 v247, v247
	v_exp_f32_e32 v248, v248
	v_exp_f32_e32 v249, v249
	v_exp_f32_e32 v250, v250
	v_exp_f32_e32 v251, v251
	v_exp_f32_e32 v252, v252
	v_exp_f32_e32 v253, v253
	v_add_f32_e32 v246, 1.0, v246
	v_add_f32_e32 v247, 1.0, v247
	v_add_f32_e32 v248, 1.0, v248
	v_add_f32_e32 v249, 1.0, v249
	v_add_f32_e32 v250, 1.0, v250
	v_add_f32_e32 v251, 1.0, v251
	v_add_f32_e32 v252, 1.0, v252
	v_add_f32_e32 v253, 1.0, v253
	v_rcp_f32_e32 v246, v246
	v_rcp_f32_e32 v247, v247
	v_rcp_f32_e32 v248, v248
	v_rcp_f32_e32 v249, v249
	v_rcp_f32_e32 v250, v250
	v_rcp_f32_e32 v251, v251
	v_rcp_f32_e32 v252, v252
	v_rcp_f32_e32 v253, v253
	v_mul_f32_e32 v230, v230, v246
	v_mul_f32_e32 v231, v231, v247
	v_mul_f32_e32 v232, v232, v248
	v_mul_f32_e32 v233, v233, v249
	v_mul_f32_e32 v234, v234, v250
	v_mul_f32_e32 v235, v235, v251
	v_mul_f32_e32 v236, v236, v252
	v_mul_f32_e32 v237, v237, v253
	v_mul_f32_e32 v230, v230, v238
	v_mul_f32_e32 v231, v231, v239
	v_mul_f32_e32 v232, v232, v240
	v_mul_f32_e32 v233, v233, v241
	v_mul_f32_e32 v234, v234, v242
	v_mul_f32_e32 v235, v235, v243
	v_mul_f32_e32 v236, v236, v244
	v_mul_f32_e32 v237, v237, v245
	v_med3_f32 v230, v230, s55, v228
	v_med3_f32 v231, v231, s55, v228
	v_med3_f32 v232, v232, s55, v228
	v_med3_f32 v233, v233, s55, v228
	v_med3_f32 v234, v234, s55, v228
	v_med3_f32 v235, v235, s55, v228
	v_med3_f32 v236, v236, s55, v228
	v_med3_f32 v237, v237, s55, v228
	v_cvt_pk_fp8_f32 v216, v230, v231
	v_cvt_pk_fp8_f32 v217, v234, v235
	v_cvt_pk_fp8_f32 v216, v232, v233 op_sel:[0,0,1]
	v_cvt_pk_fp8_f32 v217, v236, v237 op_sel:[0,0,1]
	s_nop 1
	global_store_dwordx2 v[0:1], v[216:217], off
	v_mul_f32_e32 v230, s48, v174
	v_mul_f32_e32 v231, s48, v175
	v_mul_f32_e32 v232, s48, v176
	v_mul_f32_e32 v233, s48, v177
	v_mul_f32_e32 v234, s48, v170
	v_mul_f32_e32 v235, s48, v171
	v_mul_f32_e32 v236, s48, v172
	v_mul_f32_e32 v237, s48, v173
	v_mul_f32_e32 v238, s48, v166
	v_mul_f32_e32 v239, s48, v167
	v_mul_f32_e32 v240, s48, v168
	v_mul_f32_e32 v241, s48, v169
	v_mul_f32_e32 v242, s48, v162
	v_mul_f32_e32 v243, s48, v163
	v_mul_f32_e32 v244, s48, v164
	v_mul_f32_e32 v245, s48, v165
	v_mul_f32_e32 v246, 0xbfb8aa3b, v230
	v_mul_f32_e32 v247, 0xbfb8aa3b, v231
	v_mul_f32_e32 v248, 0xbfb8aa3b, v232
	v_mul_f32_e32 v249, 0xbfb8aa3b, v233
	v_mul_f32_e32 v250, 0xbfb8aa3b, v234
	v_mul_f32_e32 v251, 0xbfb8aa3b, v235
	v_mul_f32_e32 v252, 0xbfb8aa3b, v236
	v_mul_f32_e32 v253, 0xbfb8aa3b, v237
	v_exp_f32_e32 v246, v246
	v_exp_f32_e32 v247, v247
	v_exp_f32_e32 v248, v248
	v_exp_f32_e32 v249, v249
	v_exp_f32_e32 v250, v250
	v_exp_f32_e32 v251, v251
	v_exp_f32_e32 v252, v252
	v_exp_f32_e32 v253, v253
	v_add_f32_e32 v246, 1.0, v246
	v_add_f32_e32 v247, 1.0, v247
	v_add_f32_e32 v248, 1.0, v248
	v_add_f32_e32 v249, 1.0, v249
	v_add_f32_e32 v250, 1.0, v250
	v_add_f32_e32 v251, 1.0, v251
	v_add_f32_e32 v252, 1.0, v252
	v_add_f32_e32 v253, 1.0, v253
	v_rcp_f32_e32 v246, v246
	v_rcp_f32_e32 v247, v247
	v_rcp_f32_e32 v248, v248
	v_rcp_f32_e32 v249, v249
	v_rcp_f32_e32 v250, v250
	v_rcp_f32_e32 v251, v251
	v_rcp_f32_e32 v252, v252
	v_rcp_f32_e32 v253, v253
	v_mul_f32_e32 v230, v230, v246
	v_mul_f32_e32 v231, v231, v247
	v_mul_f32_e32 v232, v232, v248
	v_mul_f32_e32 v233, v233, v249
	v_mul_f32_e32 v234, v234, v250
	v_mul_f32_e32 v235, v235, v251
	v_mul_f32_e32 v236, v236, v252
	v_mul_f32_e32 v237, v237, v253
	v_mul_f32_e32 v230, v230, v238
	v_mul_f32_e32 v231, v231, v239
	v_mul_f32_e32 v232, v232, v240
	v_mul_f32_e32 v233, v233, v241
	v_mul_f32_e32 v234, v234, v242
	v_mul_f32_e32 v235, v235, v243
	v_mul_f32_e32 v236, v236, v244
	v_mul_f32_e32 v237, v237, v245
	v_med3_f32 v230, v230, s55, v228
	v_med3_f32 v231, v231, s55, v228
	v_med3_f32 v232, v232, s55, v228
	v_med3_f32 v233, v233, s55, v228
	v_med3_f32 v234, v234, s55, v228
	v_med3_f32 v235, v235, s55, v228
	v_med3_f32 v236, v236, s55, v228
	v_med3_f32 v237, v237, s55, v228
	v_cvt_pk_fp8_f32 v216, v230, v231
	v_cvt_pk_fp8_f32 v217, v234, v235
	v_cvt_pk_fp8_f32 v216, v232, v233 op_sel:[0,0,1]
	v_cvt_pk_fp8_f32 v217, v236, v237 op_sel:[0,0,1]
	s_mov_b32 s100, 0x2000
	v_lshl_add_u64 v[218:219], v[0:1], 0, s[100:101]
	s_nop 0
	global_store_dwordx2 v[218:219], v[216:217], off
	v_mul_f32_e32 v230, s48, v158
	v_mul_f32_e32 v231, s48, v159
	v_mul_f32_e32 v232, s48, v160
	v_mul_f32_e32 v233, s48, v161
	v_mul_f32_e32 v234, s48, v154
	v_mul_f32_e32 v235, s48, v155
	v_mul_f32_e32 v236, s48, v156
	v_mul_f32_e32 v237, s48, v157
	v_mul_f32_e32 v238, s48, v150
	v_mul_f32_e32 v239, s48, v151
	v_mul_f32_e32 v240, s48, v152
	v_mul_f32_e32 v241, s48, v153
	v_mul_f32_e32 v242, s48, v146
	v_mul_f32_e32 v243, s48, v147
	v_mul_f32_e32 v244, s48, v148
	v_mul_f32_e32 v245, s48, v149
	v_mul_f32_e32 v246, 0xbfb8aa3b, v230
	v_mul_f32_e32 v247, 0xbfb8aa3b, v231
	v_mul_f32_e32 v248, 0xbfb8aa3b, v232
	v_mul_f32_e32 v249, 0xbfb8aa3b, v233
	v_mul_f32_e32 v250, 0xbfb8aa3b, v234
	v_mul_f32_e32 v251, 0xbfb8aa3b, v235
	v_mul_f32_e32 v252, 0xbfb8aa3b, v236
	v_mul_f32_e32 v253, 0xbfb8aa3b, v237
	v_exp_f32_e32 v246, v246
	v_exp_f32_e32 v247, v247
	v_exp_f32_e32 v248, v248
	v_exp_f32_e32 v249, v249
	v_exp_f32_e32 v250, v250
	v_exp_f32_e32 v251, v251
	v_exp_f32_e32 v252, v252
	v_exp_f32_e32 v253, v253
	v_add_f32_e32 v246, 1.0, v246
	v_add_f32_e32 v247, 1.0, v247
	v_add_f32_e32 v248, 1.0, v248
	v_add_f32_e32 v249, 1.0, v249
	v_add_f32_e32 v250, 1.0, v250
	v_add_f32_e32 v251, 1.0, v251
	v_add_f32_e32 v252, 1.0, v252
	v_add_f32_e32 v253, 1.0, v253
	v_rcp_f32_e32 v246, v246
	v_rcp_f32_e32 v247, v247
	v_rcp_f32_e32 v248, v248
	v_rcp_f32_e32 v249, v249
	v_rcp_f32_e32 v250, v250
	v_rcp_f32_e32 v251, v251
	v_rcp_f32_e32 v252, v252
	v_rcp_f32_e32 v253, v253
	v_mul_f32_e32 v230, v230, v246
	v_mul_f32_e32 v231, v231, v247
	v_mul_f32_e32 v232, v232, v248
	v_mul_f32_e32 v233, v233, v249
	v_mul_f32_e32 v234, v234, v250
	v_mul_f32_e32 v235, v235, v251
	v_mul_f32_e32 v236, v236, v252
	v_mul_f32_e32 v237, v237, v253
	v_mul_f32_e32 v230, v230, v238
	v_mul_f32_e32 v231, v231, v239
	v_mul_f32_e32 v232, v232, v240
	v_mul_f32_e32 v233, v233, v241
	v_mul_f32_e32 v234, v234, v242
	v_mul_f32_e32 v235, v235, v243
	v_mul_f32_e32 v236, v236, v244
	v_mul_f32_e32 v237, v237, v245
	v_med3_f32 v230, v230, s55, v228
	v_med3_f32 v231, v231, s55, v228
	v_med3_f32 v232, v232, s55, v228
	v_med3_f32 v233, v233, s55, v228
	v_med3_f32 v234, v234, s55, v228
	v_med3_f32 v235, v235, s55, v228
	v_med3_f32 v236, v236, s55, v228
	v_med3_f32 v237, v237, s55, v228
	v_cvt_pk_fp8_f32 v216, v230, v231
	v_cvt_pk_fp8_f32 v217, v234, v235
	v_cvt_pk_fp8_f32 v216, v232, v233 op_sel:[0,0,1]
	v_cvt_pk_fp8_f32 v217, v236, v237 op_sel:[0,0,1]
	s_mov_b32 s100, 0x4000
	v_lshl_add_u64 v[218:219], v[0:1], 0, s[100:101]
	s_nop 0
	global_store_dwordx2 v[218:219], v[216:217], off
	v_mul_f32_e32 v230, s48, v142
	v_mul_f32_e32 v231, s48, v143
	v_mul_f32_e32 v232, s48, v144
	v_mul_f32_e32 v233, s48, v145
	v_mul_f32_e32 v234, s48, v138
	v_mul_f32_e32 v235, s48, v139
	v_mul_f32_e32 v236, s48, v140
	v_mul_f32_e32 v237, s48, v141
	v_mul_f32_e32 v238, s48, v134
	v_mul_f32_e32 v239, s48, v135
	v_mul_f32_e32 v240, s48, v136
	v_mul_f32_e32 v241, s48, v137
	v_mul_f32_e32 v242, s48, v130
	v_mul_f32_e32 v243, s48, v131
	v_mul_f32_e32 v244, s48, v132
	v_mul_f32_e32 v245, s48, v133
	v_mul_f32_e32 v246, 0xbfb8aa3b, v230
	v_mul_f32_e32 v247, 0xbfb8aa3b, v231
	v_mul_f32_e32 v248, 0xbfb8aa3b, v232
	v_mul_f32_e32 v249, 0xbfb8aa3b, v233
	v_mul_f32_e32 v250, 0xbfb8aa3b, v234
	v_mul_f32_e32 v251, 0xbfb8aa3b, v235
	v_mul_f32_e32 v252, 0xbfb8aa3b, v236
	v_mul_f32_e32 v253, 0xbfb8aa3b, v237
	v_exp_f32_e32 v246, v246
	v_exp_f32_e32 v247, v247
	v_exp_f32_e32 v248, v248
	v_exp_f32_e32 v249, v249
	v_exp_f32_e32 v250, v250
	v_exp_f32_e32 v251, v251
	v_exp_f32_e32 v252, v252
	v_exp_f32_e32 v253, v253
	v_add_f32_e32 v246, 1.0, v246
	v_add_f32_e32 v247, 1.0, v247
	v_add_f32_e32 v248, 1.0, v248
	v_add_f32_e32 v249, 1.0, v249
	v_add_f32_e32 v250, 1.0, v250
	v_add_f32_e32 v251, 1.0, v251
	v_add_f32_e32 v252, 1.0, v252
	v_add_f32_e32 v253, 1.0, v253
	v_rcp_f32_e32 v246, v246
	v_rcp_f32_e32 v247, v247
	v_rcp_f32_e32 v248, v248
	v_rcp_f32_e32 v249, v249
	v_rcp_f32_e32 v250, v250
	v_rcp_f32_e32 v251, v251
	v_rcp_f32_e32 v252, v252
	v_rcp_f32_e32 v253, v253
	v_mul_f32_e32 v230, v230, v246
	v_mul_f32_e32 v231, v231, v247
	v_mul_f32_e32 v232, v232, v248
	v_mul_f32_e32 v233, v233, v249
	v_mul_f32_e32 v234, v234, v250
	v_mul_f32_e32 v235, v235, v251
	v_mul_f32_e32 v236, v236, v252
	v_mul_f32_e32 v237, v237, v253
	v_mul_f32_e32 v230, v230, v238
	v_mul_f32_e32 v231, v231, v239
	v_mul_f32_e32 v232, v232, v240
	v_mul_f32_e32 v233, v233, v241
	v_mul_f32_e32 v234, v234, v242
	v_mul_f32_e32 v235, v235, v243
	v_mul_f32_e32 v236, v236, v244
	v_mul_f32_e32 v237, v237, v245
	v_med3_f32 v230, v230, s55, v228
	v_med3_f32 v231, v231, s55, v228
	v_med3_f32 v232, v232, s55, v228
	v_med3_f32 v233, v233, s55, v228
	v_med3_f32 v234, v234, s55, v228
	v_med3_f32 v235, v235, s55, v228
	v_med3_f32 v236, v236, s55, v228
	v_med3_f32 v237, v237, s55, v228
	v_cvt_pk_fp8_f32 v216, v230, v231
	v_cvt_pk_fp8_f32 v217, v234, v235
	v_cvt_pk_fp8_f32 v216, v232, v233 op_sel:[0,0,1]
	v_cvt_pk_fp8_f32 v217, v236, v237 op_sel:[0,0,1]
	s_mov_b32 s100, 0x6000
	v_lshl_add_u64 v[218:219], v[0:1], 0, s[100:101]
	s_nop 0
	global_store_dwordx2 v[218:219], v[216:217], off
	v_mul_f32_e32 v230, s48, v126
	v_mul_f32_e32 v231, s48, v127
	v_mul_f32_e32 v232, s48, v128
	v_mul_f32_e32 v233, s48, v129
	v_mul_f32_e32 v234, s48, v122
	v_mul_f32_e32 v235, s48, v123
	v_mul_f32_e32 v236, s48, v124
	v_mul_f32_e32 v237, s48, v125
	v_mul_f32_e32 v238, s48, v118
	v_mul_f32_e32 v239, s48, v119
	v_mul_f32_e32 v240, s48, v120
	v_mul_f32_e32 v241, s48, v121
	v_mul_f32_e32 v242, s48, v114
	v_mul_f32_e32 v243, s48, v115
	v_mul_f32_e32 v244, s48, v116
	v_mul_f32_e32 v245, s48, v117
	v_mul_f32_e32 v246, 0xbfb8aa3b, v230
	v_mul_f32_e32 v247, 0xbfb8aa3b, v231
	v_mul_f32_e32 v248, 0xbfb8aa3b, v232
	v_mul_f32_e32 v249, 0xbfb8aa3b, v233
	v_mul_f32_e32 v250, 0xbfb8aa3b, v234
	v_mul_f32_e32 v251, 0xbfb8aa3b, v235
	v_mul_f32_e32 v252, 0xbfb8aa3b, v236
	v_mul_f32_e32 v253, 0xbfb8aa3b, v237
	v_exp_f32_e32 v246, v246
	v_exp_f32_e32 v247, v247
	v_exp_f32_e32 v248, v248
	v_exp_f32_e32 v249, v249
	v_exp_f32_e32 v250, v250
	v_exp_f32_e32 v251, v251
	v_exp_f32_e32 v252, v252
	v_exp_f32_e32 v253, v253
	v_add_f32_e32 v246, 1.0, v246
	v_add_f32_e32 v247, 1.0, v247
	v_add_f32_e32 v248, 1.0, v248
	v_add_f32_e32 v249, 1.0, v249
	v_add_f32_e32 v250, 1.0, v250
	v_add_f32_e32 v251, 1.0, v251
	v_add_f32_e32 v252, 1.0, v252
	v_add_f32_e32 v253, 1.0, v253
	v_rcp_f32_e32 v246, v246
	v_rcp_f32_e32 v247, v247
	v_rcp_f32_e32 v248, v248
	v_rcp_f32_e32 v249, v249
	v_rcp_f32_e32 v250, v250
	v_rcp_f32_e32 v251, v251
	v_rcp_f32_e32 v252, v252
	v_rcp_f32_e32 v253, v253
	v_mul_f32_e32 v230, v230, v246
	v_mul_f32_e32 v231, v231, v247
	v_mul_f32_e32 v232, v232, v248
	v_mul_f32_e32 v233, v233, v249
	v_mul_f32_e32 v234, v234, v250
	v_mul_f32_e32 v235, v235, v251
	v_mul_f32_e32 v236, v236, v252
	v_mul_f32_e32 v237, v237, v253
	v_mul_f32_e32 v230, v230, v238
	v_mul_f32_e32 v231, v231, v239
	v_mul_f32_e32 v232, v232, v240
	v_mul_f32_e32 v233, v233, v241
	v_mul_f32_e32 v234, v234, v242
	v_mul_f32_e32 v235, v235, v243
	v_mul_f32_e32 v236, v236, v244
	v_mul_f32_e32 v237, v237, v245
	v_med3_f32 v230, v230, s55, v228
	v_med3_f32 v231, v231, s55, v228
	v_med3_f32 v232, v232, s55, v228
	v_med3_f32 v233, v233, s55, v228
	v_med3_f32 v234, v234, s55, v228
	v_med3_f32 v235, v235, s55, v228
	v_med3_f32 v236, v236, s55, v228
	v_med3_f32 v237, v237, s55, v228
	v_cvt_pk_fp8_f32 v216, v230, v231
	v_cvt_pk_fp8_f32 v217, v234, v235
	v_cvt_pk_fp8_f32 v216, v232, v233 op_sel:[0,0,1]
	v_cvt_pk_fp8_f32 v217, v236, v237 op_sel:[0,0,1]
	s_mov_b32 s100, 0x10000
	v_lshl_add_u64 v[218:219], v[0:1], 0, s[100:101]
	s_nop 0
	global_store_dwordx2 v[218:219], v[216:217], off
	v_mul_f32_e32 v230, s48, v110
	v_mul_f32_e32 v231, s48, v111
	v_mul_f32_e32 v232, s48, v112
	v_mul_f32_e32 v233, s48, v113
	v_mul_f32_e32 v234, s48, v106
	v_mul_f32_e32 v235, s48, v107
	v_mul_f32_e32 v236, s48, v108
	v_mul_f32_e32 v237, s48, v109
	v_mul_f32_e32 v238, s48, v102
	v_mul_f32_e32 v239, s48, v103
	v_mul_f32_e32 v240, s48, v104
	v_mul_f32_e32 v241, s48, v105
	v_mul_f32_e32 v242, s48, v98
	v_mul_f32_e32 v243, s48, v99
	v_mul_f32_e32 v244, s48, v100
	v_mul_f32_e32 v245, s48, v101
	v_mul_f32_e32 v246, 0xbfb8aa3b, v230
	v_mul_f32_e32 v247, 0xbfb8aa3b, v231
	v_mul_f32_e32 v248, 0xbfb8aa3b, v232
	v_mul_f32_e32 v249, 0xbfb8aa3b, v233
	v_mul_f32_e32 v250, 0xbfb8aa3b, v234
	v_mul_f32_e32 v251, 0xbfb8aa3b, v235
	v_mul_f32_e32 v252, 0xbfb8aa3b, v236
	v_mul_f32_e32 v253, 0xbfb8aa3b, v237
	v_exp_f32_e32 v246, v246
	v_exp_f32_e32 v247, v247
	v_exp_f32_e32 v248, v248
	v_exp_f32_e32 v249, v249
	v_exp_f32_e32 v250, v250
	v_exp_f32_e32 v251, v251
	v_exp_f32_e32 v252, v252
	v_exp_f32_e32 v253, v253
	v_add_f32_e32 v246, 1.0, v246
	v_add_f32_e32 v247, 1.0, v247
	v_add_f32_e32 v248, 1.0, v248
	v_add_f32_e32 v249, 1.0, v249
	v_add_f32_e32 v250, 1.0, v250
	v_add_f32_e32 v251, 1.0, v251
	v_add_f32_e32 v252, 1.0, v252
	v_add_f32_e32 v253, 1.0, v253
	v_rcp_f32_e32 v246, v246
	v_rcp_f32_e32 v247, v247
	v_rcp_f32_e32 v248, v248
	v_rcp_f32_e32 v249, v249
	v_rcp_f32_e32 v250, v250
	v_rcp_f32_e32 v251, v251
	v_rcp_f32_e32 v252, v252
	v_rcp_f32_e32 v253, v253
	v_mul_f32_e32 v230, v230, v246
	v_mul_f32_e32 v231, v231, v247
	v_mul_f32_e32 v232, v232, v248
	v_mul_f32_e32 v233, v233, v249
	v_mul_f32_e32 v234, v234, v250
	v_mul_f32_e32 v235, v235, v251
	v_mul_f32_e32 v236, v236, v252
	v_mul_f32_e32 v237, v237, v253
	v_mul_f32_e32 v230, v230, v238
	v_mul_f32_e32 v231, v231, v239
	v_mul_f32_e32 v232, v232, v240
	v_mul_f32_e32 v233, v233, v241
	v_mul_f32_e32 v234, v234, v242
	v_mul_f32_e32 v235, v235, v243
	v_mul_f32_e32 v236, v236, v244
	v_mul_f32_e32 v237, v237, v245
	v_med3_f32 v230, v230, s55, v228
	v_med3_f32 v231, v231, s55, v228
	v_med3_f32 v232, v232, s55, v228
	v_med3_f32 v233, v233, s55, v228
	v_med3_f32 v234, v234, s55, v228
	v_med3_f32 v235, v235, s55, v228
	v_med3_f32 v236, v236, s55, v228
	v_med3_f32 v237, v237, s55, v228
	v_cvt_pk_fp8_f32 v216, v230, v231
	v_cvt_pk_fp8_f32 v217, v234, v235
	v_cvt_pk_fp8_f32 v216, v232, v233 op_sel:[0,0,1]
	v_cvt_pk_fp8_f32 v217, v236, v237 op_sel:[0,0,1]
	s_mov_b32 s100, 0x12000
	v_lshl_add_u64 v[218:219], v[0:1], 0, s[100:101]
	s_nop 0
	global_store_dwordx2 v[218:219], v[216:217], off
	v_mul_f32_e32 v230, s48, v94
	v_mul_f32_e32 v231, s48, v95
	v_mul_f32_e32 v232, s48, v96
	v_mul_f32_e32 v233, s48, v97
	v_mul_f32_e32 v234, s48, v90
	v_mul_f32_e32 v235, s48, v91
	v_mul_f32_e32 v236, s48, v92
	v_mul_f32_e32 v237, s48, v93
	v_mul_f32_e32 v238, s48, v86
	v_mul_f32_e32 v239, s48, v87
	v_mul_f32_e32 v240, s48, v88
	v_mul_f32_e32 v241, s48, v89
	v_mul_f32_e32 v242, s48, v82
	v_mul_f32_e32 v243, s48, v83
	v_mul_f32_e32 v244, s48, v84
	v_mul_f32_e32 v245, s48, v85
	v_mul_f32_e32 v246, 0xbfb8aa3b, v230
	v_mul_f32_e32 v247, 0xbfb8aa3b, v231
	v_mul_f32_e32 v248, 0xbfb8aa3b, v232
	v_mul_f32_e32 v249, 0xbfb8aa3b, v233
	v_mul_f32_e32 v250, 0xbfb8aa3b, v234
	v_mul_f32_e32 v251, 0xbfb8aa3b, v235
	v_mul_f32_e32 v252, 0xbfb8aa3b, v236
	v_mul_f32_e32 v253, 0xbfb8aa3b, v237
	v_exp_f32_e32 v246, v246
	v_exp_f32_e32 v247, v247
	v_exp_f32_e32 v248, v248
	v_exp_f32_e32 v249, v249
	v_exp_f32_e32 v250, v250
	v_exp_f32_e32 v251, v251
	v_exp_f32_e32 v252, v252
	v_exp_f32_e32 v253, v253
	v_add_f32_e32 v246, 1.0, v246
	v_add_f32_e32 v247, 1.0, v247
	v_add_f32_e32 v248, 1.0, v248
	v_add_f32_e32 v249, 1.0, v249
	v_add_f32_e32 v250, 1.0, v250
	v_add_f32_e32 v251, 1.0, v251
	v_add_f32_e32 v252, 1.0, v252
	v_add_f32_e32 v253, 1.0, v253
	v_rcp_f32_e32 v246, v246
	v_rcp_f32_e32 v247, v247
	v_rcp_f32_e32 v248, v248
	v_rcp_f32_e32 v249, v249
	v_rcp_f32_e32 v250, v250
	v_rcp_f32_e32 v251, v251
	v_rcp_f32_e32 v252, v252
	v_rcp_f32_e32 v253, v253
	v_mul_f32_e32 v230, v230, v246
	v_mul_f32_e32 v231, v231, v247
	v_mul_f32_e32 v232, v232, v248
	v_mul_f32_e32 v233, v233, v249
	v_mul_f32_e32 v234, v234, v250
	v_mul_f32_e32 v235, v235, v251
	v_mul_f32_e32 v236, v236, v252
	v_mul_f32_e32 v237, v237, v253
	v_mul_f32_e32 v230, v230, v238
	v_mul_f32_e32 v231, v231, v239
	v_mul_f32_e32 v232, v232, v240
	v_mul_f32_e32 v233, v233, v241
	v_mul_f32_e32 v234, v234, v242
	v_mul_f32_e32 v235, v235, v243
	v_mul_f32_e32 v236, v236, v244
	v_mul_f32_e32 v237, v237, v245
	v_med3_f32 v230, v230, s55, v228
	v_med3_f32 v231, v231, s55, v228
	v_med3_f32 v232, v232, s55, v228
	v_med3_f32 v233, v233, s55, v228
	v_med3_f32 v234, v234, s55, v228
	v_med3_f32 v235, v235, s55, v228
	v_med3_f32 v236, v236, s55, v228
	v_med3_f32 v237, v237, s55, v228
	v_cvt_pk_fp8_f32 v216, v230, v231
	v_cvt_pk_fp8_f32 v217, v234, v235
	v_cvt_pk_fp8_f32 v216, v232, v233 op_sel:[0,0,1]
	v_cvt_pk_fp8_f32 v217, v236, v237 op_sel:[0,0,1]
	s_mov_b32 s100, 0x14000
	v_lshl_add_u64 v[218:219], v[0:1], 0, s[100:101]
	s_nop 0
	global_store_dwordx2 v[218:219], v[216:217], off
	v_mul_f32_e32 v230, s48, v78
	v_mul_f32_e32 v231, s48, v79
	v_mul_f32_e32 v232, s48, v80
	v_mul_f32_e32 v233, s48, v81
	v_mul_f32_e32 v234, s48, v74
	v_mul_f32_e32 v235, s48, v75
	v_mul_f32_e32 v236, s48, v76
	v_mul_f32_e32 v237, s48, v77
	v_mul_f32_e32 v238, s48, v70
	v_mul_f32_e32 v239, s48, v71
	v_mul_f32_e32 v240, s48, v72
	v_mul_f32_e32 v241, s48, v73
	v_mul_f32_e32 v242, s48, v66
	v_mul_f32_e32 v243, s48, v67
	v_mul_f32_e32 v244, s48, v68
	v_mul_f32_e32 v245, s48, v69
	v_mul_f32_e32 v246, 0xbfb8aa3b, v230
	v_mul_f32_e32 v247, 0xbfb8aa3b, v231
	v_mul_f32_e32 v248, 0xbfb8aa3b, v232
	v_mul_f32_e32 v249, 0xbfb8aa3b, v233
	v_mul_f32_e32 v250, 0xbfb8aa3b, v234
	v_mul_f32_e32 v251, 0xbfb8aa3b, v235
	v_mul_f32_e32 v252, 0xbfb8aa3b, v236
	v_mul_f32_e32 v253, 0xbfb8aa3b, v237
	v_exp_f32_e32 v246, v246
	v_exp_f32_e32 v247, v247
	v_exp_f32_e32 v248, v248
	v_exp_f32_e32 v249, v249
	v_exp_f32_e32 v250, v250
	v_exp_f32_e32 v251, v251
	v_exp_f32_e32 v252, v252
	v_exp_f32_e32 v253, v253
	v_add_f32_e32 v246, 1.0, v246
	v_add_f32_e32 v247, 1.0, v247
	v_add_f32_e32 v248, 1.0, v248
	v_add_f32_e32 v249, 1.0, v249
	v_add_f32_e32 v250, 1.0, v250
	v_add_f32_e32 v251, 1.0, v251
	v_add_f32_e32 v252, 1.0, v252
	v_add_f32_e32 v253, 1.0, v253
	v_rcp_f32_e32 v246, v246
	v_rcp_f32_e32 v247, v247
	v_rcp_f32_e32 v248, v248
	v_rcp_f32_e32 v249, v249
	v_rcp_f32_e32 v250, v250
	v_rcp_f32_e32 v251, v251
	v_rcp_f32_e32 v252, v252
	v_rcp_f32_e32 v253, v253
	v_mul_f32_e32 v230, v230, v246
	v_mul_f32_e32 v231, v231, v247
	v_mul_f32_e32 v232, v232, v248
	v_mul_f32_e32 v233, v233, v249
	v_mul_f32_e32 v234, v234, v250
	v_mul_f32_e32 v235, v235, v251
	v_mul_f32_e32 v236, v236, v252
	v_mul_f32_e32 v237, v237, v253
	v_mul_f32_e32 v230, v230, v238
	v_mul_f32_e32 v231, v231, v239
	v_mul_f32_e32 v232, v232, v240
	v_mul_f32_e32 v233, v233, v241
	v_mul_f32_e32 v234, v234, v242
	v_mul_f32_e32 v235, v235, v243
	v_mul_f32_e32 v236, v236, v244
	v_mul_f32_e32 v237, v237, v245
	v_med3_f32 v230, v230, s55, v228
	v_med3_f32 v231, v231, s55, v228
	v_med3_f32 v232, v232, s55, v228
	v_med3_f32 v233, v233, s55, v228
	v_med3_f32 v234, v234, s55, v228
	v_med3_f32 v235, v235, s55, v228
	v_med3_f32 v236, v236, s55, v228
	v_med3_f32 v237, v237, s55, v228
	v_cvt_pk_fp8_f32 v216, v230, v231
	v_cvt_pk_fp8_f32 v217, v234, v235
	v_cvt_pk_fp8_f32 v216, v232, v233 op_sel:[0,0,1]
	v_cvt_pk_fp8_f32 v217, v236, v237 op_sel:[0,0,1]
	s_mov_b32 s100, 0x16000
	v_lshl_add_u64 v[218:219], v[0:1], 0, s[100:101]
	s_nop 0
	global_store_dwordx2 v[218:219], v[216:217], off
	s_and_b64 vcc, exec, s[4:5]
	s_cbranch_vccnz .LBB0_823
	s_andn2_b64 vcc, exec, s[6:7]
	s_cbranch_vccnz .LBB0_822
	s_barrier
	s_branch .LBB0_822
